# scan swizzle + second conversion item issued mid-step (after the second barrier) on even steps with incremental addresses and finished at the end of the next step
# speedup vs baseline: 1.0072x; 1.0072x over previous
.LBB0_422:
	s_ashr_i32 s11, s51, 16
	s_bfe_u32 s92, s51, 0x5000b
	v_readlane_b32 s76, v254, 36
	s_cmp_eq_u32 s11, 1
	v_readlane_b32 s77, v254, 37
	v_readlane_b32 s78, v254, 38
	v_readlane_b32 s79, v254, 39
	v_readlane_b32 s80, v254, 40
	v_readlane_b32 s81, v254, 41
	v_readlane_b32 s82, v254, 42
	v_readlane_b32 s83, v254, 43
	s_cselect_b32 s0, s76, s78
	s_cselect_b32 s1, s77, s79
	v_readlane_b32 s68, v254, 44
	s_cmp_lt_u32 s51, 0x10000
	v_readlane_b32 s82, v254, 58
	v_readlane_b32 s83, v254, 59
	s_cselect_b32 s1, s83, s1
	s_cselect_b32 s0, s82, s0
	s_lshl_b32 s12, s92, 24
	s_add_u32 s28, s0, s12
	s_addc_u32 s29, s1, 0
	v_readlane_b32 s69, v254, 45
	v_readlane_b32 s70, v254, 46
	v_readlane_b32 s71, v254, 47
	v_readlane_b32 s72, v254, 48
	v_readlane_b32 s73, v254, 49
	v_readlane_b32 s74, v254, 50
	v_readlane_b32 s75, v254, 51
	s_cmp_eq_u32 s92, 0
	s_cselect_b64 s[90:91], -1, 0
	v_readlane_b32 s60, v254, 20
	v_readlane_b32 s78, v254, 54
	v_readlane_b32 s79, v254, 55
	s_and_b64 s[0:1], s[90:91], exec
	v_readlane_b32 s74, v254, 34
	v_readlane_b32 s75, v254, 35
	s_cselect_b32 s30, s74, s78
	s_cselect_b32 s31, s75, s79
	s_cmp_eq_u32 s11, 3
	s_cselect_b64 s[52:53], -1, 0
	s_and_b64 s[0:1], s[52:53], exec
	s_cselect_b32 s1, s31, s29
	s_cselect_b32 s0, s30, s28
	s_and_b32 s43, s46, 0x7e0
	s_and_b32 s98, s51, 0x7c0
	s_lshl_b32 s98, s98, 13
	s_lshl_b32 s40, s43, 2
	s_add_u32 s98, s98, s40
	s_add_u32 s100, s0, s98
	s_addc_u32 s101, s1, 0
	global_load_dwordx4 v[152:155], v250, s[100:101]
	v_add_u32_e32 v253, 0x2000, v250
	global_load_dwordx4 v[156:159], v253, s[100:101]
	v_add_u32_e32 v252, 0x4000, v250
	global_load_dwordx4 v[160:163], v252, s[100:101]
	v_add_u32_e32 v253, 0x6000, v250
	global_load_dwordx4 v[164:167], v253, s[100:101]
	v_add_u32_e32 v252, 0x8000, v250
	global_load_dwordx4 v[168:171], v252, s[100:101]
	v_add_u32_e32 v253, 0xa000, v250
	global_load_dwordx4 v[172:175], v253, s[100:101]
	v_add_u32_e32 v252, 0xc000, v250
	global_load_dwordx4 v[176:179], v252, s[100:101]
	v_add_u32_e32 v253, 0xe000, v250
	global_load_dwordx4 v[246:249], v253, s[100:101]
	s_lshr_b32 s98, s49, 9
	s_lshl_b32 s98, s98, 8
	s_cmp_lt_u32 s7, 60
	s_cselect_b32 s0, s98, 0
	s_cselect_b32 s1, s7, 0
	s_and_b32 s1, s1, 1
	s_cmp_lg_u32 s1, 0
	s_cselect_b64 s[94:95], -1, 0
	s_add_i32 s0, s0, s44
	s_lshl_b32 s0, s0, 3
	v_readlane_b32 s1, v255, 15
	s_add_i32 s28, s1, s0
	s_bfe_u32 s93, s28, 0x5000b
	s_ashr_i32 s57, s28, 16
	s_lshl_b32 s13, s93, 22
	s_cmp_eq_u32 s57, 3
	s_cselect_b64 s[96:97], -1, 0
	s_cmp_eq_u32 s93, 0
	s_cselect_b64 s[0:1], -1, 0
	s_lshl_b32 s34, s28, 5
	s_and_b32 s37, s34, 0x7e0
	s_and_b32 s36, s28, 0x7c0
	s_mov_b32 s38, s86
	s_and_b32 s98, s7, 1
	s_cmp_gt_u32 s7, 59
	s_cselect_b32 s98, 1, s98
	s_sub_u32 s99, s7, 2
	s_cmp_lt_u32 s99, 53
	s_cselect_b32 s98, 1, s98
	s_cmp_lg_u32 s98, 0
	v_readlane_b32 s76, v254, 52
	v_readlane_b32 s77, v254, 53
	v_readlane_b32 s80, v254, 56
	v_readlane_b32 s81, v254, 57
	v_readlane_b32 s61, v254, 21
	v_readlane_b32 s62, v254, 22
	v_readlane_b32 s63, v254, 23
	v_readlane_b32 s64, v254, 24
	v_readlane_b32 s65, v254, 25
	v_readlane_b32 s66, v254, 26
	v_readlane_b32 s67, v254, 27
	v_readlane_b32 s68, v254, 28
	v_readlane_b32 s69, v254, 29
	v_readlane_b32 s70, v254, 30
	v_readlane_b32 s71, v254, 31
	v_readlane_b32 s72, v254, 32
	v_readlane_b32 s73, v254, 33
	s_cbranch_scc1 .LBB0_424
	v_readlane_b32 s80, v254, 36
	s_cmp_eq_u32 s57, 1
	v_readlane_b32 s81, v254, 37
	v_readlane_b32 s82, v254, 38
	v_readlane_b32 s83, v254, 39
	s_cselect_b32 s29, s80, s82
	s_cselect_b32 s30, s81, s83
	v_readlane_b32 s68, v254, 44
	s_cmp_lt_u32 s28, 0x10000
	v_readlane_b32 s82, v254, 58
	v_readlane_b32 s83, v254, 59
	s_cselect_b32 s28, s83, s30
	s_cselect_b32 s29, s82, s29
	s_lshl_b32 s30, s13, 2
	v_readlane_b32 s69, v254, 45
	v_readlane_b32 s70, v254, 46
	v_readlane_b32 s71, v254, 47
	v_readlane_b32 s72, v254, 48
	v_readlane_b32 s73, v254, 49
	v_readlane_b32 s74, v254, 50
	v_readlane_b32 s75, v254, 51
	s_add_u32 s30, s29, s30
	s_addc_u32 s31, s28, 0
	v_readlane_b32 s60, v254, 20
	v_readlane_b32 s78, v254, 54
	v_readlane_b32 s79, v254, 55
	s_and_b64 s[28:29], s[0:1], exec
	v_readlane_b32 s74, v254, 34
	v_readlane_b32 s75, v254, 35
	s_cselect_b32 s60, s74, s78
	s_cselect_b32 vcc_lo, s75, s79
	s_and_b64 s[28:29], s[96:97], exec
	s_cselect_b32 s29, vcc_lo, s31
	s_cselect_b32 s28, s60, s30
	s_lshl_b32 s98, s36, 13
	s_lshl_b32 s40, s37, 2
	s_add_u32 s98, s98, s40
	s_add_u32 s100, s28, s98
	s_addc_u32 s101, s29, 0
	v_writelane_b32 v255, s100, 48
	v_writelane_b32 v255, s101, 49
	global_load_dwordx4 v[2:5], v250, s[100:101]
	v_add_u32_e32 v253, 0x2000, v250
	global_load_dwordx4 v[6:9], v253, s[100:101]
	v_add_u32_e32 v252, 0x4000, v250
	global_load_dwordx4 v[10:13], v252, s[100:101]
	v_add_u32_e32 v253, 0x6000, v250
	global_load_dwordx4 v[14:17], v253, s[100:101]
	v_add_u32_e32 v252, 0x8000, v250
	global_load_dwordx4 v[18:21], v252, s[100:101]
	v_add_u32_e32 v253, 0xa000, v250
	global_load_dwordx4 v[22:25], v253, s[100:101]
	v_add_u32_e32 v252, 0xc000, v250
	global_load_dwordx4 v[26:29], v252, s[100:101]
	v_add_u32_e32 v253, 0xe000, v250
	global_load_dwordx4 v[116:119], v253, s[100:101]
	v_readlane_b32 s84, v254, 40
	v_readlane_b32 s85, v254, 41
	v_readlane_b32 s86, v254, 42
	v_readlane_b32 s87, v254, 43
	v_readlane_b32 s76, v254, 52
	v_readlane_b32 s77, v254, 53
	v_readlane_b32 s80, v254, 56
	v_readlane_b32 s81, v254, 57
	v_readlane_b32 s61, v254, 21
	v_readlane_b32 s62, v254, 22
	v_readlane_b32 s63, v254, 23
	v_readlane_b32 s64, v254, 24
	v_readlane_b32 s65, v254, 25
	v_readlane_b32 s66, v254, 26
	v_readlane_b32 s67, v254, 27
	v_readlane_b32 s68, v254, 28
	v_readlane_b32 s69, v254, 29
	v_readlane_b32 s70, v254, 30
	v_readlane_b32 s71, v254, 31
	v_readlane_b32 s72, v254, 32
	v_readlane_b32 s73, v254, 33

.Lqk_done:
.LBB0_447:
	v_lshl_add_u32 v184, v132, 2, s60
	s_waitcnt lgkmcnt(0)
	ds_read_b128 v[102:105], v184
	v_readlane_b32 s28, v255, 38
	v_readlane_b32 s29, v255, 39
	s_waitcnt lgkmcnt(0)
	v_sub_f32_e32 v102, v102, v183
	v_mul_f32_e32 v102, 0x3fb8aa3b, v102
	v_exp_f32_e32 v102, v102
	v_sub_f32_e32 v103, v103, v183
	v_sub_f32_e32 v104, v104, v183
	v_mul_f32_e32 v103, 0x3fb8aa3b, v103
	v_mul_f32_e32 v98, v98, v102
	v_sub_f32_e32 v102, v105, v183
	v_exp_f32_e32 v103, v103
	v_mul_f32_e32 v104, 0x3fb8aa3b, v104
	v_mul_f32_e32 v102, 0x3fb8aa3b, v102
	v_exp_f32_e32 v104, v104
	v_exp_f32_e32 v102, v102
	v_mul_f32_e32 v99, v99, v103
	v_cndmask_b32_e64 v98, v98, 0, s[28:29]
	v_cndmask_b32_e64 v99, 0, v99, s[14:15]
	v_mul_f32_e32 v100, v100, v104
	v_mul_f32_e32 v101, v101, v102
	v_cndmask_b32_e64 v100, v100, 0, s[16:17]
	v_cndmask_b32_e64 v101, v101, 0, s[18:19]
	v_cvt_pk_bf16_f32 v98, v98, v99
	v_cvt_pk_bf16_f32 v99, v100, v101
	ds_write_b64 v144, v[98:99]
	ds_read_b128 v[98:101], v184 offset:64
	s_mul_i32 s28, s6, 0x4620
	s_add_i32 s28, s28, 0
	s_add_i32 s28, s28, 0x10800
	s_waitcnt lgkmcnt(0)
	v_sub_f32_e32 v98, v98, v183
	v_sub_f32_e32 v99, v99, v183
	v_mul_f32_e32 v98, 0x3fb8aa3b, v98
	v_mul_f32_e32 v99, 0x3fb8aa3b, v99
	v_exp_f32_e32 v98, v98
	v_exp_f32_e32 v99, v99
	v_mul_f32_e32 v94, v94, v98
	v_mul_f32_e32 v95, v95, v99
	v_sub_f32_e32 v98, v100, v183
	v_sub_f32_e32 v99, v101, v183
	v_mul_f32_e32 v98, 0x3fb8aa3b, v98
	v_mul_f32_e32 v99, 0x3fb8aa3b, v99
	v_exp_f32_e32 v98, v98
	v_exp_f32_e32 v99, v99
	v_cndmask_b32_e64 v94, v94, 0, s[20:21]
	v_cndmask_b32_e64 v95, v95, 0, s[22:23]
	v_mul_f32_e32 v96, v96, v98
	v_mul_f32_e32 v97, v97, v99
	v_cndmask_b32_e64 v96, v96, 0, s[24:25]
	v_cndmask_b32_e64 v97, v97, 0, s[26:27]
	v_cvt_pk_bf16_f32 v94, v94, v95
	v_cvt_pk_bf16_f32 v95, v96, v97
	ds_write_b64 v145, v[94:95]
	s_waitcnt lgkmcnt(0)
	s_barrier
	s_sub_u32 s98, s7, 2
	s_cmp_lt_u32 s98, 53
	s_cbranch_scc0 .Lcv2m_skip
	s_bitcmp1_b32 s7, 0
	s_cbranch_scc1 .Lcv2m_skip
	v_readlane_b32 s100, v255, 48
	v_readlane_b32 s101, v255, 49
	s_add_u32 s100, s100, 0x1000000
	s_addc_u32 s101, s101, 0
	v_writelane_b32 v255, s100, 48
	v_writelane_b32 v255, s101, 49
	global_load_dwordx4 v[2:5], v250, s[100:101]
	v_add_u32_e32 v253, 0x2000, v250
	global_load_dwordx4 v[6:9], v253, s[100:101]
	v_add_u32_e32 v252, 0x4000, v250
	global_load_dwordx4 v[10:13], v252, s[100:101]
	v_add_u32_e32 v253, 0x6000, v250
	global_load_dwordx4 v[14:17], v253, s[100:101]
	v_add_u32_e32 v252, 0x8000, v250
	global_load_dwordx4 v[18:21], v252, s[100:101]
	v_add_u32_e32 v253, 0xa000, v250
	global_load_dwordx4 v[22:25], v253, s[100:101]
	v_add_u32_e32 v252, 0xc000, v250
	global_load_dwordx4 v[26:29], v252, s[100:101]
	v_add_u32_e32 v253, 0xe000, v250
	global_load_dwordx4 v[116:119], v253, s[100:101]
.Lcv2m_skip:
	v_add3_u32 v183, s28, v135, v131
	ds_read_b128 v[94:97], v183 offset:16896
	ds_read_b128 v[98:101], v149
	ds_read_b128 v[102:105], v183 offset:16960
	ds_read_b128 v[184:187], v149 offset:64
	s_waitcnt lgkmcnt(2)
	v_mfma_f32_16x16x32_bf16 v[94:97], v[94:97], v[98:101], 0
	ds_read_b128 v[188:191], v183 offset:17024
	ds_read_b128 v[192:195], v149 offset:128
	s_waitcnt lgkmcnt(2)
	v_mfma_f32_16x16x32_bf16 v[94:97], v[102:105], v[184:187], v[94:97]
	ds_read_b128 v[102:105], v183 offset:17088
	ds_read_b128 v[200:203], v149 offset:192
	s_waitcnt lgkmcnt(2)
	v_mfma_f32_16x16x32_bf16 v[94:97], v[188:191], v[192:195], v[94:97]
	ds_read_b128 v[188:191], v183 offset:17152
	ds_read_b128 v[204:207], v149 offset:256
	s_waitcnt lgkmcnt(2)
	v_mfma_f32_16x16x32_bf16 v[94:97], v[102:105], v[200:203], v[94:97]
	ds_read_b128 v[102:105], v183 offset:17216
	ds_read_b128 v[208:211], v149 offset:320
	s_waitcnt lgkmcnt(2)
	v_mfma_f32_16x16x32_bf16 v[94:97], v[188:191], v[204:207], v[94:97]
	ds_read_b128 v[188:191], v183 offset:17280
	ds_read_b128 v[212:215], v149 offset:384
	s_waitcnt lgkmcnt(2)
	v_mfma_f32_16x16x32_bf16 v[94:97], v[102:105], v[208:211], v[94:97]
	ds_read_b128 v[102:105], v183 offset:17344
	ds_read_b128 v[216:219], v149 offset:448
	v_add_u32_e32 v183, v133, v32
	s_waitcnt lgkmcnt(2)
	v_mfma_f32_16x16x32_bf16 v[94:97], v[188:191], v[212:215], v[94:97]
	v_add_u32_e32 v188, v138, v136
	ds_read_b64_tr_b16 v[190:191], v188 offset:320
	ds_read_b64_tr_b16 v[188:189], v188
	ds_read_b128 v[224:227], v183
	s_waitcnt lgkmcnt(3)
	v_mfma_f32_16x16x32_bf16 v[94:97], v[102:105], v[216:219], v[94:97]
	s_waitcnt lgkmcnt(0)
	v_mfma_f32_16x16x32_bf16 v[188:191], v[188:191], v[224:227], 0
	s_nop 5
	v_add_u32_e32 v95, v138, v137
	ds_read_b64_tr_b16 v[102:103], v95 offset:64
	ds_read_b64_tr_b16 v[104:105], v95 offset:384
	v_add_u32_e32 v95, v139, v136
	ds_read_b64_tr_b16 v[230:231], v95 offset:320
	ds_read_b64_tr_b16 v[228:229], v95
	ds_read_b128 v[232:235], v146
	v_add_u32_e32 v95, v139, v137
	s_waitcnt lgkmcnt(3)
	v_mfma_f32_16x16x32_bf16 v[102:105], v[102:105], v[224:227], 0
	ds_read_b64_tr_b16 v[224:225], v95 offset:64
	ds_read_b64_tr_b16 v[226:227], v95 offset:384
	v_add3_u32 v95, s28, v134, v131
	s_waitcnt lgkmcnt(2)
	v_mfma_f32_16x16x32_bf16 v[188:191], v[228:231], v[232:235], v[188:191]
	ds_read_b128 v[228:231], v95
	s_waitcnt lgkmcnt(1)
	v_mfma_f32_16x16x32_bf16 v[102:105], v[224:227], v[232:235], v[102:105]
	ds_read_b128 v[224:227], v95 offset:64
	s_waitcnt lgkmcnt(1)
	v_mfma_f32_16x16x32_bf16 v[96:99], v[228:231], v[98:101], 0
	ds_read_b128 v[228:231], v95 offset:128
	s_waitcnt lgkmcnt(1)
	v_mfma_f32_16x16x32_bf16 v[96:99], v[224:227], v[184:187], v[96:99]
	ds_read_b128 v[184:187], v95 offset:192
	s_waitcnt lgkmcnt(1)
	v_mfma_f32_16x16x32_bf16 v[96:99], v[228:231], v[192:195], v[96:99]
	ds_read_b128 v[192:195], v95 offset:256
	s_waitcnt lgkmcnt(1)
	v_mfma_f32_16x16x32_bf16 v[96:99], v[184:187], v[200:203], v[96:99]
	ds_read_b128 v[184:187], v95 offset:320
	s_waitcnt lgkmcnt(1)
	v_mfma_f32_16x16x32_bf16 v[96:99], v[192:195], v[204:207], v[96:99]
	ds_read2st64_b32 v[104:105], v182 offset0:2 offset1:3
	ds_read_b128 v[192:195], v95 offset:384
	s_waitcnt lgkmcnt(1)
	v_fmac_f32_e32 v102, v94, v104
	ds_bpermute_b32 v182, v151, v102
	v_mfma_f32_16x16x32_bf16 v[96:99], v[184:187], v[208:211], v[96:99]
	ds_read_b128 v[100:103], v95 offset:448
	s_waitcnt lgkmcnt(2)
	v_mfma_f32_16x16x32_bf16 v[94:97], v[192:195], v[212:215], v[96:99]
	s_waitcnt lgkmcnt(0)
	v_mfma_f32_16x16x32_bf16 v[94:97], v[100:103], v[216:219], v[94:97]
	s_nop 2
	v_max_f32_e64 v98, |v182|, |v182|
	v_max_f32_e32 v99, v105, v105
	v_max_f32_e32 v98, v98, v99
	v_div_scale_f32 v99, s[28:29], v98, v98, 1.0
	v_rcp_f32_e32 v105, v99
	v_fma_f32 v94, v94, v104, v188
	v_fma_f32 v95, v95, v104, v189
	v_fma_f32 v96, v96, v104, v190
	v_fma_f32 v100, -v99, v105, 1.0
	v_fmac_f32_e32 v105, v100, v105
	v_div_scale_f32 v100, vcc, 1.0, v98, 1.0
	v_mul_f32_e32 v101, v100, v105
	v_fma_f32 v102, -v99, v101, v100
	v_fmac_f32_e32 v101, v102, v105
	v_fma_f32 v99, -v99, v101, v100
	v_div_fmas_f32 v99, v99, v105, v101
	v_div_fixup_f32 v98, v99, v98, 1.0
	v_fmac_f32_e32 v191, v97, v104
	v_mov_b32_e32 v182, s60
	v_mul_f32_e32 v94, v94, v98
	v_mul_f32_e32 v95, v95, v98
	v_mul_f32_e32 v96, v96, v98
	v_mul_f32_e32 v97, v191, v98
	v_cvt_pk_bf16_f32 v200, v94, v95
	v_cvt_pk_bf16_f32 v201, v96, v97
	ds_read_b32 v196, v182 offset:1280
	ds_read_b64_tr_b16 v[94:95], v147
	ds_read_b64_tr_b16 v[98:99], v147 offset:32
	ds_read_b64_tr_b16 v[102:103], v147 offset:64
	ds_read_b64_tr_b16 v[184:185], v30 offset:35904
	ds_read_b64_tr_b16 v[182:183], v148 offset:33792
	ds_read_b64_tr_b16 v[96:97], v147 offset:320
	ds_read_b64_tr_b16 v[100:101], v147 offset:352
	ds_read_b64_tr_b16 v[104:105], v147 offset:384
	ds_read_b64_tr_b16 v[186:187], v147 offset:2560
	ds_read_b64_tr_b16 v[188:189], v148 offset:33824
	ds_read_b64_tr_b16 v[192:193], v147 offset:2944
	ds_read_b64_tr_b16 v[190:191], v30 offset:35936
	s_waitcnt lgkmcnt(12)
	v_pk_mul_f32 v[88:89], v[88:89], v[196:197] op_sel_hi:[1,0]
	v_pk_mul_f32 v[86:87], v[86:87], v[196:197] op_sel_hi:[1,0]
	v_pk_mul_f32 v[84:85], v[84:85], v[196:197] op_sel_hi:[1,0]
	v_pk_mul_f32 v[82:83], v[82:83], v[196:197] op_sel_hi:[1,0]
	v_pk_mul_f32 v[76:77], v[76:77], v[196:197] op_sel_hi:[1,0]
	v_pk_mul_f32 v[74:75], v[74:75], v[196:197] op_sel_hi:[1,0]
	v_pk_mul_f32 v[80:81], v[80:81], v[196:197] op_sel_hi:[1,0]
	v_pk_mul_f32 v[78:79], v[78:79], v[196:197] op_sel_hi:[1,0]
	v_pk_mul_f32 v[72:73], v[72:73], v[196:197] op_sel_hi:[1,0]
	v_pk_mul_f32 v[70:71], v[70:71], v[196:197] op_sel_hi:[1,0]
	v_pk_mul_f32 v[68:69], v[68:69], v[196:197] op_sel_hi:[1,0]
	v_pk_mul_f32 v[66:67], v[66:67], v[196:197] op_sel_hi:[1,0]
	s_waitcnt lgkmcnt(6)
	v_mfma_f32_16x16x32_bf16 v[86:89], v[182:185], v[94:97], v[86:89]
	s_add_i32 s28, s47, 0xffffff00
	s_cmp_lt_u32 s7, 4
	s_cselect_b32 s7, s47, s28
	s_waitcnt lgkmcnt(5)
	v_mfma_f32_16x16x32_bf16 v[82:85], v[182:185], v[98:101], v[82:85]
	s_waitcnt lgkmcnt(4)
	v_mfma_f32_16x16x32_bf16 v[74:77], v[182:185], v[102:105], v[74:77]
	ds_read_b64_tr_b16 v[182:183], v148 offset:50688
	ds_read_b64_tr_b16 v[194:195], v148 offset:50720
	ds_read_b64_tr_b16 v[184:185], v30 offset:52800
	s_waitcnt lgkmcnt(3)
	v_mfma_f32_16x16x32_bf16 v[78:81], v[188:191], v[94:97], v[78:81]
	v_mfma_f32_16x16x32_bf16 v[70:73], v[188:191], v[98:101], v[70:73]
	v_add_u32_e32 v98, s7, v130
	s_movk_i32 s7, 0xfff
	s_cselect_b32 s7, 0xff, s7
	v_mfma_f32_16x16x32_bf16 v[66:69], v[188:191], v[102:105], v[66:69]
	ds_read_b64_tr_b16 v[188:189], v147 offset:2880
	ds_read_b64_tr_b16 v[96:97], v147 offset:2912
	ds_read_b64_tr_b16 v[190:191], v147 offset:2624
	ds_read_b64_tr_b16 v[94:95], v147 offset:2592
	ds_read_b64_tr_b16 v[196:197], v30 offset:52832
	v_sub_u32_e32 v99, s7, v98
	v_cndmask_b32_e64 v98, v99, v98, s[2:3]
	s_cselect_b32 s7, s45, s48
	v_add_u32_e32 v98, s7, v98
	v_ashrrev_i32_e32 v99, 31, v98
	s_waitcnt lgkmcnt(4)
	v_mfma_f32_16x16x32_bf16 v[86:89], v[182:185], v[186:189], v[86:89]
	s_xor_b32 s6, s6, 1
	s_mul_i32 s7, s6, 0x4620
	s_waitcnt lgkmcnt(1)
	v_mfma_f32_16x16x32_bf16 v[82:85], v[182:185], v[94:97], v[82:85]
	v_mfma_f32_16x16x32_bf16 v[74:77], v[182:185], v[190:193], v[74:77]
	s_waitcnt lgkmcnt(0)
	v_mfma_f32_16x16x32_bf16 v[78:81], v[194:197], v[186:189], v[78:81]
	v_mfma_f32_16x16x32_bf16 v[70:73], v[194:197], v[94:97], v[70:73]
	v_lshlrev_b64 v[94:95], 11, v[98:99]
	v_lshl_add_u64 v[94:95], v[110:111], 0, v[94:95]
	global_store_dwordx2 v[94:95], v[200:201], off
	v_mfma_f32_16x16x32_bf16 v[66:69], v[194:197], v[190:193], v[66:69]
	v_add_u32_e32 v94, s7, v140
	v_cvt_pk_bf16_f32 v96, v86, v87
	v_cvt_pk_bf16_f32 v97, v88, v89
	v_add3_u32 v95, v94, v135, v31
	ds_write_b64 v95, v[96:97]
	v_cvt_pk_bf16_f32 v96, v82, v83
	v_cvt_pk_bf16_f32 v97, v84, v85
	ds_write_b64 v95, v[96:97] offset:8448
	s_and_saveexec_b64 s[28:29], s[8:9]
	s_cbranch_execz .LBB0_449
	v_cvt_pk_bf16_f32 v96, v74, v75
	v_cvt_pk_bf16_f32 v97, v76, v77
	ds_write_b64 v94, v[96:97] offset:16896

.Lcvw_done:
	v_cvt_pk_bf16_f32 v152, v152, v156
	v_cvt_pk_bf16_f32 v156, v153, v157
	v_cvt_pk_bf16_f32 v238, v154, v158
	v_cvt_pk_bf16_f32 v242, v155, v159
	v_cvt_pk_bf16_f32 v153, v160, v164
	v_cvt_pk_bf16_f32 v157, v161, v165
	v_cvt_pk_bf16_f32 v239, v162, v166
	v_cvt_pk_bf16_f32 v243, v163, v167
	v_cvt_pk_bf16_f32 v154, v168, v172
	v_cvt_pk_bf16_f32 v158, v169, v173
	v_cvt_pk_bf16_f32 v240, v170, v174
	v_cvt_pk_bf16_f32 v244, v171, v175
	v_cvt_pk_bf16_f32 v155, v176, v246
	v_cvt_pk_bf16_f32 v159, v177, v247
	v_cvt_pk_bf16_f32 v241, v178, v248
	v_cvt_pk_bf16_f32 v245, v179, v249
	global_store_dwordx4 v251, v[152:155], s[100:101]
	global_store_dwordx4 v251, v[156:159], s[100:101] offset:128
	global_store_dwordx4 v251, v[238:241], s[100:101] offset:256
	global_store_dwordx4 v251, v[242:245], s[100:101] offset:384
	s_andn2_b64 vcc, exec, s[94:95]
	s_mov_b32 s86, s38
	v_readlane_b32 s81, v254, 37
	v_readlane_b32 s82, v254, 38
	v_readlane_b32 s83, v254, 39
	v_readlane_b32 s84, v254, 40
	v_readlane_b32 s85, v254, 41
	s_cbranch_vccnz .LBB0_410
	s_sub_u32 s98, s47, 192
	s_cmp_lt_u32 s98, 0xd40
	s_cbranch_scc0 .Lcv2f_slow
	v_readlane_b32 s100, v255, 50
	v_readlane_b32 s101, v255, 51
	s_add_u32 s100, s100, 0x800000
	s_addc_u32 s101, s101, 0
	s_branch .Lcv2f_go
.Lcv2f_slow:
	s_lshl_b32 s7, s13, 1
	s_add_u32 s7, s35, s7
	s_addc_u32 s11, s33, 0
	s_lshl_b32 s28, s93, 24
	s_add_u32 s28, s56, s28
	s_addc_u32 s29, s39, 0
	s_cmp_eq_u32 s57, 2
	s_cselect_b32 s7, s7, s28
	s_cselect_b32 s11, s11, s29
	s_and_b64 s[0:1], s[0:1], exec
	s_mov_b32 s0, 0x2400000
	v_readlane_b32 s72, v254, 36
	s_cselect_b32 s0, s0, 0x4300000
	v_readlane_b32 s78, v254, 42
	v_readlane_b32 s79, v254, 43
	s_add_u32 s28, s78, s0
	s_addc_u32 s29, s79, 0
	s_and_b64 s[0:1], s[96:97], exec
	s_cselect_b32 s1, s29, s11
	s_cselect_b32 s0, s28, s7
	s_lshl_b32 s7, s37, 1
	s_and_b32 s11, s34, 0x60
	s_lshl_b32 s28, s57, 7
	s_and_b32 s7, s7, 0xf00
	s_or_b32 s11, s28, s11
	s_add_i32 s11, s11, s7
	s_cmp_gt_i32 s57, 1
	s_cselect_b32 s7, s37, s11
	s_ashr_i32 s11, s7, 3
	s_andn2_b32 s11, s11, 31
	s_lshr_b32 s28, s36, 6
	s_or_b32 s28, s11, s28
	s_ashr_i32 s29, s28, 31
	s_lshl_b64 s[28:29], s[28:29], 8
	s_and_b32 s7, s7, 0xe0
	s_or_b32 s7, s28, s7
	v_readlane_b32 s73, v254, 37
	v_readlane_b32 s74, v254, 38
	v_readlane_b32 s75, v254, 39
	v_readlane_b32 s76, v254, 40
	v_readlane_b32 s77, v254, 41
	s_mov_b32 s100, s7
	s_mov_b32 s101, s29
	s_lshl_b64 s[100:101], s[100:101], 7
	s_add_u32 s100, s100, s0
	s_addc_u32 s101, s101, s1
